# baseline (speedup 1.0000x reference)
.LBB2_5:
	s_setprio 0
	ds_read_b128 v[102:105], v114 offset:8192
	ds_read_b128 v[106:109], v114 offset:10240
	ds_read_b128 v[110:113], v114 offset:12288
	v_exp_f32_e32 v69, v46
	v_exp_f32_e32 v71, v47
	v_exp_f32_e32 v73, v48
	v_exp_f32_e32 v75, v49
	ds_read_b128 v[46:49], v114 offset:14336
	v_exp_f32_e32 v42, v42
	v_exp_f32_e32 v43, v43
	v_exp_f32_e32 v44, v44
	v_exp_f32_e32 v45, v45
	v_cvt_pk_f16_f32 v76, v69, v71
	v_cvt_pk_f16_f32 v77, v73, v75
	v_cvt_pk_f16_f32 v78, v42, v43
	v_cvt_pk_f16_f32 v79, v44, v45
	ds_read_b128 v[42:45], v115 offset:8192
	v_exp_f32_e32 v38, v38
	v_exp_f32_e32 v39, v39
	s_waitcnt lgkmcnt(4)
	v_mfma_f32_16x16x32_f16 v[26:29], v[102:105], v[76:79], v[26:29]
	v_exp_f32_e32 v40, v40
	v_exp_f32_e32 v41, v41
	s_waitcnt lgkmcnt(3)
	v_mfma_f32_16x16x32_f16 v[22:25], v[106:109], v[76:79], v[22:25]
	ds_read_b128 v[102:105], v115 offset:10240
	v_exp_f32_e32 v34, v34
	v_exp_f32_e32 v35, v35
	s_waitcnt lgkmcnt(3)
	v_mfma_f32_16x16x32_f16 v[18:21], v[110:113], v[76:79], v[18:21]
	ds_read_b128 v[106:109], v115 offset:12288
	v_exp_f32_e32 v36, v36
	v_exp_f32_e32 v37, v37
	s_waitcnt lgkmcnt(3)
	v_mfma_f32_16x16x32_f16 v[10:13], v[46:49], v[76:79], v[10:13]
	ds_read_b128 v[110:113], v115 offset:14336
	v_mfma_f32_16x16x32_f16 v[14:17], v[116:119], v[76:79], v[14:17]
	v_cvt_pk_f16_f32 v37, v36, v37
	v_cvt_pk_f16_f32 v36, v34, v35
	v_cvt_pk_f16_f32 v35, v40, v41
	v_cvt_pk_f16_f32 v34, v38, v39
	s_mov_b64 s[38:39], 0
	s_waitcnt lgkmcnt(3)
	v_mfma_f32_16x16x32_f16 v[26:29], v[42:45], v[34:37], v[26:29]
	s_waitcnt lgkmcnt(2)
	v_mfma_f32_16x16x32_f16 v[22:25], v[102:105], v[34:37], v[22:25]
	s_waitcnt lgkmcnt(1)
	v_mfma_f32_16x16x32_f16 v[18:21], v[106:109], v[34:37], v[18:21]
	s_waitcnt lgkmcnt(0)
	v_mfma_f32_16x16x32_f16 v[10:13], v[110:113], v[34:37], v[10:13]
	v_mfma_f32_16x16x32_f16 v[14:17], v[116:119], v[34:37], v[14:17]

.LBB2_7:
	s_add_i32 s37, s64, -1
	s_and_b32 s37, s37, 1
	s_lshl_b32 s37, s37, 14
	s_add_i32 s48, s40, s64
	s_add_i32 s48, s48, -1
	v_or_b32_e32 v114, s37, v57
	v_or_b32_e32 v115, s37, v81
	s_cmp_eq_u32 s55, 0
	s_cbranch_scc1 .Lattn_prio_keep
	s_setprio 1
.Lattn_prio_keep:
	s_cmp_gt_u32 s48, s63
	s_waitcnt vmcnt(0) lgkmcnt(0)
	s_barrier
